# MLA loop: running softmax reference kept in one register, rare path updates it in place (common path loses the v_cndmask, the copy and the flag moves)
# speedup vs baseline: 1.0026x; 1.0026x over previous
.LBB0_565:
	s_waitcnt lgkmcnt(4)
	v_mfma_scale_f32_32x32x64_f8f6f4 v[96:111], v[96:103], v[120:127], 0, v205, v205 op_sel_hi:[0,0,0]
	v_fma_f32 v80, v80, s40, -v192
	v_fma_f32 v81, v81, s40, -v192
	v_fma_f32 v84, v84, s40, -v192
	v_fma_f32 v85, v85, s40, -v192
	v_fma_f32 v88, v88, s40, -v192
	v_fma_f32 v89, v89, s40, -v192
	v_fma_f32 v92, v92, s40, -v192
	v_fma_f32 v93, v93, s40, -v192
	v_exp_f32_e32 v80, v80
	v_exp_f32_e32 v81, v81
	v_exp_f32_e32 v84, v84
	v_exp_f32_e32 v85, v85
	v_exp_f32_e32 v88, v88
	v_exp_f32_e32 v89, v89
	s_waitcnt lgkmcnt(2)
	v_mfma_scale_f32_32x32x64_f8f6f4 v[96:111], v[156:163], v[128:135], v[96:111], v205, v205 op_sel_hi:[0,0,0]
	v_exp_f32_e32 v92, v92
	v_exp_f32_e32 v93, v93
	v_fma_f32 v82, v82, s40, -v192
	v_fma_f32 v83, v83, s40, -v192
	v_fma_f32 v86, v86, s40, -v192
	v_fma_f32 v87, v87, s40, -v192
	v_fma_f32 v90, v90, s40, -v192
	v_fma_f32 v91, v91, s40, -v192
	v_fma_f32 v94, v94, s40, -v192
	v_fma_f32 v95, v95, s40, -v192
	v_exp_f32_e32 v82, v82
	v_exp_f32_e32 v83, v83
	v_exp_f32_e32 v86, v86
	v_exp_f32_e32 v87, v87
	v_exp_f32_e32 v90, v90
	s_waitcnt lgkmcnt(0)
	v_mfma_scale_f32_32x32x64_f8f6f4 v[96:111], v[148:155], v[136:143], v[96:111], v205, v205 op_sel_hi:[0,0,0]
	v_lshl_add_u32 v240, s23, 14, v211
	ds_read_b128 v[224:227], v240
	ds_read_b128 v[228:231], v240 offset:16
	ds_read_b128 v[232:235], v240 offset:2560
	ds_read_b128 v[236:239], v240 offset:2576
	v_exp_f32_e32 v91, v91
	v_exp_f32_e32 v94, v94
	v_exp_f32_e32 v95, v95
	v_cvt_pk_fp8_f32 v148, v80, v81
	v_cvt_pk_fp8_f32 v149, v84, v85
	v_cvt_pk_fp8_f32 v150, v88, v89
	v_cvt_pk_fp8_f32 v151, v92, v93
	v_cvt_pk_fp8_f32 v148, v82, v83 op_sel:[0,0,1]
	v_cvt_pk_fp8_f32 v149, v86, v87 op_sel:[0,0,1]
	v_cvt_pk_fp8_f32 v150, v90, v91 op_sel:[0,0,1]
	v_cvt_pk_fp8_f32 v151, v94, v95 op_sel:[0,0,1]
	s_nop 0
	s_waitcnt lgkmcnt(2)
	v_mfma_scale_f32_32x32x64_f8f6f4 v[48:63], v[144:151], v[224:231], v[48:63], v205, v205 op_sel_hi:[0,0,0]
	ds_read_b128 v[80:83], v240 offset:5120
	ds_read_b128 v[84:87], v240 offset:5136
	ds_read_b128 v[152:155], v240 offset:7680
	ds_read_b128 v[156:159], v240 offset:7696
	s_waitcnt lgkmcnt(4)
	v_mfma_scale_f32_32x32x64_f8f6f4 v[32:47], v[144:151], v[232:239], v[32:47], v205, v205 op_sel_hi:[0,0,0]
	v_max_f32_e32 v88, v96, v97
	v_max3_f32 v88, v88, v98, v99
	v_max3_f32 v88, v88, v100, v101
	v_max3_f32 v88, v88, v102, v103
	v_max3_f32 v88, v88, v104, v105
	v_max3_f32 v88, v88, v106, v107
	s_waitcnt lgkmcnt(2)
	v_mfma_scale_f32_32x32x64_f8f6f4 v[16:31], v[144:151], v[80:87], v[16:31], v205, v205 op_sel_hi:[0,0,0]
	v_max3_f32 v88, v88, v108, v109
	v_max3_f32 v88, v88, v110, v111
	v_mov_b32_e32 v89, v88
	s_nop 1
	v_permlane32_swap_b32_e32 v88, v89
	v_max_f32_e32 v80, v88, v89
	v_fma_f32 v81, v80, s40, -v192
	v_cmp_ge_f32_e32 vcc, s70, v81
	s_waitcnt lgkmcnt(0)
	v_mfma_scale_f32_32x32x64_f8f6f4 v[0:15], v[144:151], v[152:159], v[0:15], v205, v205 op_sel_hi:[0,0,0]
	s_cmp_eq_u64 vcc, exec
	s_cbranch_scc0 .Lmla_rare_a0
	v_mov_b32_e32 v88, 1.0

.LBB0_570:
	s_waitcnt lgkmcnt(4)
	v_mfma_scale_f32_32x32x64_f8f6f4 v[80:95], v[80:87], v[120:127], 0, v205, v205 op_sel_hi:[0,0,0]
	s_cmp_ge_u32 s18, s20
	s_waitcnt lgkmcnt(2)
	v_mfma_scale_f32_32x32x64_f8f6f4 v[80:95], v[104:111], v[128:135], v[80:95], v205, v205 op_sel_hi:[0,0,0]
	s_waitcnt lgkmcnt(0)
	v_mfma_scale_f32_32x32x64_f8f6f4 v[80:95], v[96:103], v[136:143], v[80:95], v205, v205 op_sel_hi:[0,0,0]
	s_nop 15
	s_nop 3
	v_max_f32_e32 v96, v80, v81
	v_max3_f32 v96, v96, v82, v83
	v_max3_f32 v96, v96, v84, v85
	v_max3_f32 v96, v96, v86, v87
	v_max3_f32 v96, v96, v88, v89
	v_max3_f32 v96, v96, v90, v91
	v_max3_f32 v96, v96, v92, v93
	v_max3_f32 v96, v96, v94, v95
	v_mov_b32_e32 v97, v96
	s_nop 1
	v_permlane32_swap_b32_e32 v96, v97
	v_max_f32_e32 v96, v96, v97
	v_fma_f32 v97, v96, s40, -v192
	v_cmp_ge_f32_e32 vcc, s70, v97
	s_cbranch_scc1 .LBB0_577
	s_xor_b32 s25, s23, 1
	s_lshl_b32 s18, s25, 15
	s_add_i32 s26, s18, 0
	v_add3_u32 v97, s26, v212, v190
	s_waitcnt vmcnt(1)
	ds_write_b128 v97, v[168:171]
	s_and_saveexec_b64 s[18:19], s[0:1]
	v_add3_u32 v97, s26, v215, v188
	ds_write_b128 v97, v[164:167]
	s_or_b64 exec, exec, s[18:19]
	v_lshl_add_u32 v97, s25, 14, v207
	s_cmp_ge_u32 s78, s74
	s_waitcnt vmcnt(0)
	ds_write_b128 v97, v[172:175]
	s_cbranch_scc1 .LBB0_577
	s_cmp_lt_u32 s78, s77
	s_cselect_b32 s18, 0, s77
	s_cselect_b32 s19, s76, s75
	s_lshl_b32 s18, s18, 6
	s_sub_i32 s25, s19, s18
	s_add_i32 s25, s25, s22
	v_add_u32_e32 v97, s25, v210
	v_mad_i64_i32 v[98:99], s[18:19], v97, s64, v[194:195]
	global_load_dwordx4 v[168:171], v[98:99], off
	s_and_saveexec_b64 s[18:19], s[0:1]
	s_cbranch_execz .LBB0_576
	v_add_u32_e32 v97, s25, v213
	v_mad_i64_i32 v[98:99], s[26:27], v97, s64, v[196:197]
	global_load_dwordx4 v[164:167], v[98:99], off

.LBB0_577:
	s_cmp_eq_u64 vcc, exec
	s_cbranch_scc0 .Lmla_rare_b0
	v_mov_b32_e32 v191, 1.0

.Lmla_rare_a0:
	v_fmamk_f32 v80, v80, 0x3dd53b94, v202
	v_max_f32_e32 v81, v192, v80
	v_sub_f32_e32 v80, v192, v81
	v_exp_f32_e32 v88, v80
	v_mov_b32_e32 v192, v81
	s_branch .Lmla_back_a0
.Lmla_rare_b0:
	v_mul_f32_e32 v96, 0x3dd53b94, v96
	v_add_f32_e32 v96, 0xc0a00000, v96
	v_max_f32_e32 v189, v192, v96
	v_sub_f32_e32 v96, v192, v189
	v_exp_f32_e32 v191, v96
	v_mov_b32_e32 v192, v189
	s_branch .Lmla_back_b0

.LBB0_1875:
	s_waitcnt lgkmcnt(4)
	v_mfma_scale_f32_32x32x64_f8f6f4 v[96:111], v[96:103], v[120:127], 0, v207, v207 op_sel_hi:[0,0,0]
	v_fma_f32 v80, v80, s38, -v194
	v_fma_f32 v81, v81, s38, -v194
	v_fma_f32 v84, v84, s38, -v194
	v_fma_f32 v85, v85, s38, -v194
	v_fma_f32 v88, v88, s38, -v194
	v_fma_f32 v89, v89, s38, -v194
	v_fma_f32 v92, v92, s38, -v194
	v_fma_f32 v93, v93, s38, -v194
	v_exp_f32_e32 v80, v80
	v_exp_f32_e32 v81, v81
	v_exp_f32_e32 v84, v84
	v_exp_f32_e32 v85, v85
	v_exp_f32_e32 v88, v88
	v_exp_f32_e32 v89, v89
	s_waitcnt lgkmcnt(2)
	v_mfma_scale_f32_32x32x64_f8f6f4 v[96:111], v[156:163], v[128:135], v[96:111], v207, v207 op_sel_hi:[0,0,0]
	v_exp_f32_e32 v92, v92
	v_exp_f32_e32 v93, v93
	v_fma_f32 v82, v82, s38, -v194
	v_fma_f32 v83, v83, s38, -v194
	v_fma_f32 v86, v86, s38, -v194
	v_fma_f32 v87, v87, s38, -v194
	v_fma_f32 v90, v90, s38, -v194
	v_fma_f32 v91, v91, s38, -v194
	v_fma_f32 v94, v94, s38, -v194
	v_fma_f32 v95, v95, s38, -v194
	v_exp_f32_e32 v82, v82
	v_exp_f32_e32 v83, v83
	v_exp_f32_e32 v86, v86
	v_exp_f32_e32 v87, v87
	v_exp_f32_e32 v90, v90
	s_waitcnt lgkmcnt(0)
	v_mfma_scale_f32_32x32x64_f8f6f4 v[96:111], v[148:155], v[136:143], v[96:111], v207, v207 op_sel_hi:[0,0,0]
	v_lshl_add_u32 v240, s24, 14, v209
	ds_read_b128 v[224:227], v240
	ds_read_b128 v[228:231], v240 offset:16
	ds_read_b128 v[232:235], v240 offset:2560
	ds_read_b128 v[236:239], v240 offset:2576
	v_exp_f32_e32 v91, v91
	v_exp_f32_e32 v94, v94
	v_exp_f32_e32 v95, v95
	v_cvt_pk_fp8_f32 v148, v80, v81
	v_cvt_pk_fp8_f32 v149, v84, v85
	v_cvt_pk_fp8_f32 v150, v88, v89
	v_cvt_pk_fp8_f32 v151, v92, v93
	v_cvt_pk_fp8_f32 v148, v82, v83 op_sel:[0,0,1]
	v_cvt_pk_fp8_f32 v149, v86, v87 op_sel:[0,0,1]
	v_cvt_pk_fp8_f32 v150, v90, v91 op_sel:[0,0,1]
	v_cvt_pk_fp8_f32 v151, v94, v95 op_sel:[0,0,1]
	s_nop 0
	s_waitcnt lgkmcnt(2)
	v_mfma_scale_f32_32x32x64_f8f6f4 v[48:63], v[144:151], v[224:231], v[48:63], v207, v207 op_sel_hi:[0,0,0]
	ds_read_b128 v[80:83], v240 offset:5120
	ds_read_b128 v[84:87], v240 offset:5136
	ds_read_b128 v[152:155], v240 offset:7680
	ds_read_b128 v[156:159], v240 offset:7696
	s_waitcnt lgkmcnt(4)
	v_mfma_scale_f32_32x32x64_f8f6f4 v[32:47], v[144:151], v[232:239], v[32:47], v207, v207 op_sel_hi:[0,0,0]
	v_max_f32_e32 v88, v96, v97
	v_max3_f32 v88, v88, v98, v99
	v_max3_f32 v88, v88, v100, v101
	v_max3_f32 v88, v88, v102, v103
	v_max3_f32 v88, v88, v104, v105
	v_max3_f32 v88, v88, v106, v107
	s_waitcnt lgkmcnt(2)
	v_mfma_scale_f32_32x32x64_f8f6f4 v[16:31], v[144:151], v[80:87], v[16:31], v207, v207 op_sel_hi:[0,0,0]
	v_max3_f32 v88, v88, v108, v109
	v_max3_f32 v88, v88, v110, v111
	v_mov_b32_e32 v89, v88
	s_nop 1
	v_permlane32_swap_b32_e32 v88, v89
	v_max_f32_e32 v80, v88, v89
	v_fma_f32 v81, v80, s38, -v194
	v_cmp_ge_f32_e32 vcc, s68, v81
	s_waitcnt lgkmcnt(0)
	v_mfma_scale_f32_32x32x64_f8f6f4 v[0:15], v[144:151], v[152:159], v[0:15], v207, v207 op_sel_hi:[0,0,0]
	s_cmp_eq_u64 vcc, exec
	s_cbranch_scc0 .Lmla_rare_a1
	v_mov_b32_e32 v88, 1.0

.LBB0_1886:
	s_cmp_eq_u64 s[4:5], s[20:21]
	s_cbranch_scc0 .Lmla_rare_b1
	v_mov_b32_e32 v193, 1.0

.Lmla_rare_a1:
	v_fmamk_f32 v80, v80, 0x3dd53b94, v204
	v_max_f32_e32 v81, v194, v80
	v_sub_f32_e32 v80, v194, v81
	v_exp_f32_e32 v88, v80
	v_mov_b32_e32 v194, v81
	s_branch .Lmla_back_a1
.Lmla_rare_b1:
	v_mul_f32_e32 v96, 0x3dd53b94, v96
	v_add_f32_e32 v96, 0xc0a00000, v96
	v_max_f32_e32 v191, v194, v96
	v_sub_f32_e32 v96, v194, v191
	v_exp_f32_e32 v193, v96
	v_mov_b32_e32 v194, v191
	s_branch .Lmla_back_b1
